# baseline (speedup 1.0000x reference)
.LBB0_28:
	s_load_dwordx2 s[58:59], s[0:1], 0x20
	s_load_dwordx2 s[56:57], s[0:1], 0x38
	v_and_b32_e32 v3, 63, v0
	v_cmp_gt_u32_e32 vcc, 64, v0
	v_mbcnt_lo_u32_b32 v29, -1, 0
	s_waitcnt lgkmcnt(0)
	s_barrier
	s_and_saveexec_b64 s[14:15], vcc
	s_cbranch_execz .LBB0_37
	v_mov_b32_e32 v4, 0x1dd00
	v_lshl_add_u32 v4, v0, 4, v4
	s_waitcnt vmcnt(0)
	ds_read_b128 v[4:7], v4
	s_waitcnt lgkmcnt(0)
	v_add_u32_e32 v27, v5, v4
	v_add_u32_e32 v21, v27, v6
	v_add_u32_e32 v31, v21, v7
	s_add_i32 s3, s18, 3
	s_and_b32 s3, s3, -4
	s_mulk_i32 s2, 0x314
	s_add_i32 s3, s3, s2
	v_mov_b32_e32 v32, v31
	v_sub_u32_e32 v9, s3, v31
	v_lshlrev_b32_e32 v30, 2, v0
	v_add_u32_dpp v32, v32, v32 row_shr:1 row_mask:0xf bank_mask:0xf
	s_nop 1
	v_add_u32_dpp v32, v32, v32 row_shr:2 row_mask:0xf bank_mask:0xf
	s_nop 1
	v_add_u32_dpp v32, v32, v32 row_shr:4 row_mask:0xf bank_mask:0xf
	s_nop 1
	v_add_u32_dpp v32, v32, v32 row_shr:8 row_mask:0xf bank_mask:0xf
	s_nop 1
	v_add_u32_dpp v32, v32, v32 row_bcast:15 row_mask:0xa bank_mask:0xf
	s_nop 1
	v_add_u32_dpp v32, v32, v32 row_bcast:31 row_mask:0xc bank_mask:0xf
	s_nop 1
	v_add_u32_e32 v8, v32, v9
	v_cmp_gt_i32_e32 vcc, s33, v30
	s_and_saveexec_b64 s[2:3], vcc
	v_mov_b32_e32 v9, 0x26500
	v_lshl_add_u32 v31, v30, 3, v9
	v_mov_b32_e32 v9, v4
	ds_write_b64 v31, v[8:9]
	s_or_b64 exec, exec, s[2:3]
	v_or_b32_e32 v9, 1, v30
	v_cmp_gt_i32_e32 vcc, s33, v9
	s_and_saveexec_b64 s[2:3], vcc
	v_mov_b32_e32 v9, 0x26508
	v_lshl_add_u32 v9, v30, 3, v9
	v_add_u32_e32 v4, v8, v4
	ds_write_b64 v9, v[4:5]
	s_or_b64 exec, exec, s[2:3]
	v_or_b32_e32 v4, 2, v30
	v_cmp_gt_i32_e32 vcc, s33, v4
	s_and_saveexec_b64 s[2:3], vcc
	v_mov_b32_e32 v4, 0x26510
	v_lshl_add_u32 v9, v30, 3, v4
	v_add_u32_e32 v4, v27, v8
	v_mov_b32_e32 v5, v6
	ds_write_b64 v9, v[4:5]
	s_or_b64 exec, exec, s[2:3]
	v_or_b32_e32 v4, 3, v30
	v_cmp_gt_i32_e32 vcc, s33, v4
	s_and_b64 exec, exec, vcc
	v_mov_b32_e32 v4, 0x26518
	v_lshl_add_u32 v4, v30, 3, v4
	v_add_u32_e32 v6, v21, v8
	ds_write_b64 v4, v[6:7]
